# P4: static s_setprio 1 for waves 4-7 over the indexer phase
# speedup vs baseline: 1.0049x; 1.0021x over previous
.LBB0_410:
	s_cmp_lt_i32 s46, 5
	s_cselect_b64 s[6:7], -1, 0
	s_and_b64 s[4:5], s[6:7], s[4:5]
	s_andn2_b64 vcc, exec, s[4:5]
	s_cbranch_vccnz .LBB0_427
	s_mov_b64 s[6:7], s[0:1]
	v_mov_b32_e32 v2, v0
	s_cmpk_gt_i32 s2, 0xff
	s_cbranch_scc1 .LBB0_427
	s_cmp_lt_u32 s52, 4
	s_cbranch_scc1 .Lp4prio
	s_setprio 1
.Lp4prio:
	v_lshrrev_b32_e32 v1, 1, v2
	v_and_b32_e32 v4, 3, v2
	v_and_or_b32 v1, v1, 12, v4
	v_ashrrev_i32_e32 v10, 3, v2
	v_lshrrev_b32_e32 v3, 5, v2
	v_bfe_u32 v178, v2, 5, 1
	v_bfe_u32 v180, v2, 2, 1
	v_lshlrev_b32_e32 v4, 6, v1
	v_and_b32_e32 v8, 31, v2
	v_lshlrev_b32_e32 v1, 4, v2
	v_xor_b32_e32 v5, v10, v2
	v_and_b32_e32 v2, 7, v2
	s_lshl_b32 s3, s52, 3
	v_ashrrev_i32_e32 v11, 31, v10
	v_bitop3_b32 v3, v3, v2, 1 bitop3:0x6c
	s_add_u32 s6, s44, 0x98898000
	v_lshlrev_b64 v[12:13], 7, v[10:11]
	v_lshlrev_b32_e32 v179, 4, v3
	v_bitop3_b32 v3, v178, v2, 2 bitop3:0x36
	s_addc_u32 s7, s45, 0
	v_mov_b32_e32 v183, 0
	v_lshlrev_b32_e32 v6, 3, v178
	v_lshl_add_u64 v[14:15], s[44:45], 0, v[12:13]
	v_and_b32_e32 v182, 0x70, v1
	v_lshlrev_b32_e32 v5, 4, v5
	v_lshlrev_b32_e32 v181, 4, v3
	v_bitop3_b32 v3, v178, v2, 4 bitop3:0x36
	v_lshl_add_u64 v[14:15], v[14:15], 0, v[182:183]
	s_mov_b64 s[8:9], 0x98498000
	v_lshlrev_b32_e32 v1, 7, v10
	v_and_b32_e32 v5, 0x70, v5
	s_add_u32 s24, s44, 0x70098000
	v_or_b32_e32 v186, s3, v178
	v_lshlrev_b32_e32 v187, 4, v3
	v_bitop3_b32 v3, v178, v2, 6 bitop3:0x36
	v_lshl_or_b32 v12, v2, 4, v12
	s_mov_b64 s[10:11], 0x9849c000
	v_lshlrev_b32_e32 v190, 1, v8
	v_lshlrev_b32_e32 v200, 1, v4
	v_lshlrev_b32_e32 v204, 1, v6
	v_lshl_add_u64 v[184:185], v[14:15], 0, s[8:9]
	s_addc_u32 s25, s45, 0
	s_mov_b32 s9, 0
	v_add3_u32 v1, 0, v5, v1
	v_lshlrev_b32_e32 v191, 4, v3
	v_lshl_add_u32 v193, v8, 7, 0
	v_lshl_add_u64 v[188:189], v[12:13], 0, s[10:11]
	v_lshlrev_b32_e32 v192, 1, v186
	v_or_b32_e32 v194, 0x70098040, v190
	v_mov_b32_e32 v195, v183
	v_or_b32_e32 v196, 0x700a0000, v190
	v_mov_b32_e32 v197, v183
	s_movk_i32 s26, 0x4e00
	v_mov_b64_e32 v[198:199], s[44:45]
	v_mov_b32_e32 v218, 0x4e00
	v_mov_b32_e32 v202, v200
	v_mov_b32_e32 v203, v183
	v_mov_b32_e32 v206, v204
	v_mov_b32_e32 v207, v183
	s_mov_b64 s[10:11], 0x4909a400
	s_mov_b32 s27, 0x4909a000
	s_mov_b32 s28, 0x70098000
	s_mov_b64 s[12:13], 0x2000
	s_mov_b64 s[14:15], 0x80
	v_lshlrev_b32_e32 v182, 1, v8
	v_mov_b32_e32 v219, 0x4080000
	s_mov_b32 s29, s2
	s_mov_b32 s30, s2
	s_branch .LBB0_414

.LBB0_427:
	s_setprio 0
	s_cmp_gt_i32 s47, 5
	s_cselect_b64 s[6:7], -1, 0
	s_and_b64 s[4:5], s[4:5], s[6:7]
	s_andn2_b64 vcc, exec, s[4:5]
	s_cbranch_vccnz .LBB0_477
	s_waitcnt vmcnt(0)
	v_cmp_eq_u32_e32 vcc, 0, v0
	s_waitcnt vmcnt(0)
	s_barrier
	s_and_saveexec_b64 s[4:5], vcc
	s_cbranch_execz .LBB0_476
	s_add_i32 s3, 0, 0x23ff0
	v_mov_b32_e32 v1, s3
	s_waitcnt vmcnt(0) expcnt(0) lgkmcnt(0)
	ds_read_b32 v3, v1
	s_add_i32 s3, 0, 0x23ff4
	v_mov_b32_e32 v1, s3
	ds_read_b32 v1, v1
	s_waitcnt lgkmcnt(1)
	v_cmp_ne_u32_e32 vcc, 0, v3
	s_cbranch_vccnz .LBB0_444
	s_load_dwordx2 s[12:13], s[50:51], 0x4
	s_add_u32 s8, s44, 0x1000
	s_addc_u32 s9, s45, 0
	s_add_u32 s10, s44, 0x1100
	s_addc_u32 s11, s45, 0
	s_waitcnt lgkmcnt(0)
	s_mul_i32 s3, s12, s48
	s_add_u32 s12, s44, 0x1200
	s_mul_i32 s3, s3, s13
	s_addc_u32 s13, s45, 0
	s_add_u32 s14, s44, 0x1300
	s_addc_u32 s15, s45, 0
	s_mov_b32 s22, 1
	v_mov_b32_e32 v17, 0
	s_branch .LBB0_432
